# E8: E7 + sel far-tile loop: next-tile address SALU + LDS-DMA issue moved from the loop top (right after the barrier) to below the first LDS fragment reads
# speedup vs baseline: 1.0134x; 1.0023x over previous
.LBB0_693:
	s_lshl_b32 s0, s83, 14
	s_add_i32 s0, s0, 0
	v_add_u32_e32 v0, s0, v140
	ds_read_b128 v[70:73], v0
	ds_read_b128 v[74:77], v0 offset:4096
	ds_read_b128 v[78:81], v197
	ds_read_b128 v[82:85], v197 offset:4096
	ds_read_b128 v[86:89], v0 offset:8192
	s_add_i32 s1, s37, s33
	s_add_i32 s1, s1, -1
	ds_read_b128 v[94:97], v0 offset:12288
	s_add_i32 s98, s33, -1
	s_cmp_ge_u32 s98, s86
	s_cbranch_scc1 .Lr687_skip
	s_cmp_ge_i32 s33, s42
	s_mov_b64 s[98:99], -1
	s_cbranch_scc0 .Lr687_a
	s_add_i32 s98, s8, s33
	s_cmp_ge_i32 s98, s43
	s_cselect_b32 s99, s82, 0
	s_add_i32 s22, s98, s99
	s_mov_b64 s[98:99], 0
.Lr687_a:
	s_andn2_b64 vcc, exec, s[98:99]
	s_cbranch_vccnz .Lr687_b
	s_add_i32 s22, s3, s37
.Lr687_b:
	s_lshl_b32 s98, s22, 6
	s_lshl_b32 s22, s22, 13
	s_ashr_i32 s23, s22, 31
	s_lshl_b64 s[22:23], s[22:23], 1
	s_add_u32 s22, s46, s22
	s_addc_u32 s23, s47, s23
	s_cmp_eq_u32 s83, 0
	s_cselect_b32 s99, 0x4000, 0
	s_cselect_b32 s30, s79, 0x8000
	s_add_i32 s99, s28, s99
	v_lshl_add_u64 v[240:241], s[22:23], 0, v[102:103]
	s_mov_b32 m0, s99
	s_nop 0
	global_load_lds_dwordx4 v[240:241], off
	s_add_i32 m0, s99, 0x400
	s_ashr_i32 s99, s98, 31
	s_lshl_b64 s[98:99], s[98:99], 1
	s_add_u32 s98, s44, s98
	v_lshl_add_u64 v[240:241], s[22:23], 0, v[108:109]
	s_addc_u32 s99, s45, s99
	s_add_i32 s22, s28, s30
	global_load_lds_dwordx4 v[240:241], off
	v_lshl_add_u64 v[240:241], s[98:99], 0, v[106:107]
	s_mov_b32 m0, s22
	s_nop 0
	global_load_lds_dwordx4 v[240:241], off
	v_lshl_add_u64 v[240:241], s[98:99], 0, v[112:113]
	s_add_i32 m0, s22, 0x400
	s_nop 0
	global_load_lds_dwordx4 v[240:241], off
.Lr687_skip:
	s_waitcnt lgkmcnt(0)
	v_mfma_f32_16x16x32_bf16 v[90:93], v[70:73], v[78:81], 0
	v_mfma_f32_16x16x32_bf16 v[70:73], v[70:73], v[82:85], 0
	v_add_u32_e32 v0, s0, v143
	ds_read_b128 v[198:201], v0
	ds_read_b128 v[202:205], v197 offset:1024
	ds_read_b128 v[206:209], v197 offset:5120
	v_mfma_f32_16x16x32_bf16 v[98:101], v[74:77], v[78:81], 0
	v_mfma_f32_16x16x32_bf16 v[74:77], v[74:77], v[82:85], 0
	v_mfma_f32_16x16x32_bf16 v[210:213], v[86:89], v[78:81], 0
	ds_read_b128 v[214:217], v0 offset:4096
	v_mfma_f32_16x16x32_bf16 v[86:89], v[86:89], v[82:85], 0
	v_mfma_f32_16x16x32_bf16 v[78:81], v[94:97], v[78:81], 0
	v_mfma_f32_16x16x32_bf16 v[82:85], v[94:97], v[82:85], 0
	ds_read_b128 v[94:97], v0 offset:8192
	s_waitcnt lgkmcnt(3)
	v_mfma_f32_16x16x32_bf16 v[90:93], v[198:201], v[202:205], v[90:93]
	s_waitcnt lgkmcnt(2)
	v_mfma_f32_16x16x32_bf16 v[70:73], v[198:201], v[206:209], v[70:73]
	ds_read_b128 v[198:201], v0 offset:12288
	v_add_u32_e32 v0, s0, v144
	s_waitcnt lgkmcnt(2)
	v_mfma_f32_16x16x32_bf16 v[98:101], v[214:217], v[202:205], v[98:101]
	v_mfma_f32_16x16x32_bf16 v[74:77], v[214:217], v[206:209], v[74:77]
	ds_read_b128 v[214:217], v0
	ds_read_b128 v[218:221], v197 offset:2048
	ds_read_b128 v[222:225], v197 offset:6144
	s_waitcnt lgkmcnt(4)
	v_mfma_f32_16x16x32_bf16 v[210:213], v[94:97], v[202:205], v[210:213]
	v_mfma_f32_16x16x32_bf16 v[86:89], v[94:97], v[206:209], v[86:89]
	ds_read_b128 v[94:97], v0 offset:4096
	s_waitcnt lgkmcnt(4)
	v_mfma_f32_16x16x32_bf16 v[78:81], v[198:201], v[202:205], v[78:81]
	ds_read_b128 v[202:205], v0 offset:8192
	v_mfma_f32_16x16x32_bf16 v[82:85], v[198:201], v[206:209], v[82:85]
	s_waitcnt lgkmcnt(3)
	v_mfma_f32_16x16x32_bf16 v[90:93], v[214:217], v[218:221], v[90:93]
	ds_read_b128 v[198:201], v0 offset:12288
	s_waitcnt lgkmcnt(3)
	v_mfma_f32_16x16x32_bf16 v[70:73], v[214:217], v[222:225], v[70:73]
	v_add_u32_e32 v0, s0, v145
	s_waitcnt lgkmcnt(2)
	v_mfma_f32_16x16x32_bf16 v[206:209], v[94:97], v[218:221], v[98:101]
	v_mfma_f32_16x16x32_bf16 v[74:77], v[94:97], v[222:225], v[74:77]
	ds_read_b128 v[94:97], v0
	ds_read_b128 v[214:217], v197 offset:3072
	ds_read_b128 v[228:231], v197 offset:7168
	s_waitcnt lgkmcnt(4)
	v_mfma_f32_16x16x32_bf16 v[210:213], v[202:205], v[218:221], v[210:213]
	v_mfma_f32_16x16x32_bf16 v[86:89], v[202:205], v[222:225], v[86:89]
	ds_read_b128 v[202:205], v0 offset:4096
	ds_read_b128 v[232:235], v0 offset:8192
	s_waitcnt lgkmcnt(5)
	v_mfma_f32_16x16x32_bf16 v[218:221], v[198:201], v[218:221], v[78:81]
	v_mfma_f32_16x16x32_bf16 v[198:201], v[198:201], v[222:225], v[82:85]
	s_waitcnt lgkmcnt(3)
	v_mfma_f32_16x16x32_bf16 v[82:85], v[94:97], v[214:217], v[90:93]
	ds_read_b128 v[222:225], v0 offset:12288
	s_waitcnt lgkmcnt(3)
	v_mfma_f32_16x16x32_bf16 v[98:101], v[94:97], v[228:231], v[70:73]
	s_waitcnt lgkmcnt(2)
	v_mfma_f32_16x16x32_bf16 v[78:81], v[202:205], v[214:217], v[206:209]
	v_mfma_f32_16x16x32_bf16 v[94:97], v[202:205], v[228:231], v[74:77]
	s_waitcnt lgkmcnt(1)
	v_mfma_f32_16x16x32_bf16 v[74:77], v[232:235], v[214:217], v[210:213]
	v_mfma_f32_16x16x32_bf16 v[90:93], v[232:235], v[228:231], v[86:89]
	s_nop 0
	v_max_f32_e32 v2, v82, v83
	s_waitcnt lgkmcnt(0)
	v_mfma_f32_16x16x32_bf16 v[70:73], v[222:225], v[214:217], v[218:221]
	s_ashr_i32 s22, s1, 5
	v_max_f32_e32 v125, v84, v85
	v_mfma_f32_16x16x32_bf16 v[86:89], v[222:225], v[228:231], v[198:201]
	v_lshl_add_u32 v134, s22, 2, v148
	ds_read_b32 v5, v196 offset:508
	ds_read_b32 v0, v134
	v_max_f32_e32 v137, v80, v81
	v_max3_f32 v137, v78, v79, v137
	v_max3_f32 v2, v2, v125, v137
	v_max_f32_e32 v125, v76, v77
	v_max_f32_e32 v137, v72, v73
	s_lshl_b32 s0, 1, s1
	v_max3_f32 v125, v74, v75, v125
	v_max3_f32 v137, v70, v71, v137
	s_waitcnt lgkmcnt(0)
	v_and_b32_e32 v0, s0, v0
	v_max3_f32 v2, v2, v125, v137
	v_cmp_ne_u32_e32 vcc, 0, v0
	v_mov_b32_e32 v0, v2
	s_nop 1
	v_permlane16_swap_b32_e32 v2, v0
	v_max_f32_e32 v0, v2, v0
	v_mov_b32_e32 v2, v0
	s_nop 1
	v_permlane32_swap_b32_e32 v0, v2
	v_cndmask_b32_e32 v137, v159, v5, vcc
	v_max_f32_e32 v0, v0, v2
	v_fmamk_f32 v0, v0, 0x3fb8aa3b, v137
	v_max_f32_e32 v125, v133, v0
	v_sub_f32_e32 v0, v133, v125
	v_exp_f32_e32 v2, v0
	s_nop 0
	v_cmp_neq_f32_e32 vcc, 1.0, v2
	s_cbranch_vccz .LBB0_695
	v_pk_mul_f32 v[68:69], v[68:69], v[2:3] op_sel_hi:[1,0]
	v_pk_mul_f32 v[66:67], v[66:67], v[2:3] op_sel_hi:[1,0]
	v_pk_mul_f32 v[64:65], v[64:65], v[2:3] op_sel_hi:[1,0]
	v_pk_mul_f32 v[62:63], v[62:63], v[2:3] op_sel_hi:[1,0]
	v_pk_mul_f32 v[60:61], v[60:61], v[2:3] op_sel_hi:[1,0]
	v_pk_mul_f32 v[58:59], v[58:59], v[2:3] op_sel_hi:[1,0]
	v_pk_mul_f32 v[56:57], v[56:57], v[2:3] op_sel_hi:[1,0]
	v_pk_mul_f32 v[54:55], v[54:55], v[2:3] op_sel_hi:[1,0]
	v_pk_mul_f32 v[52:53], v[52:53], v[2:3] op_sel_hi:[1,0]
	v_pk_mul_f32 v[50:51], v[50:51], v[2:3] op_sel_hi:[1,0]
	v_pk_mul_f32 v[48:49], v[48:49], v[2:3] op_sel_hi:[1,0]
	v_pk_mul_f32 v[46:47], v[46:47], v[2:3] op_sel_hi:[1,0]
	v_pk_mul_f32 v[44:45], v[44:45], v[2:3] op_sel_hi:[1,0]
	v_pk_mul_f32 v[42:43], v[42:43], v[2:3] op_sel_hi:[1,0]
	v_pk_mul_f32 v[40:41], v[40:41], v[2:3] op_sel_hi:[1,0]
	v_pk_mul_f32 v[38:39], v[38:39], v[2:3] op_sel_hi:[1,0]

.LBB0_700:
	s_lshl_b32 s8, s36, 19
	s_cmp_gt_i32 s82, s86
	s_cbranch_scc1 .LBB0_781
	s_sub_i32 s36, s2, s43
	s_sub_i32 s84, 0, s42
	s_cmp_ge_i32 s82, s42
	s_mov_b64 s[0:1], -1
	s_cbranch_scc0 .LBB0_704
	s_branch .LBB0_703
	s_nop 0
	s_nop 0
	s_nop 0
	s_nop 0
	s_nop 0
	s_nop 0
	s_nop 0
	s_nop 0
	s_nop 0
	s_nop 0
	s_nop 0
	s_nop 0
	s_nop 0
	s_nop 0
	s_nop 0
	s_nop 0
	s_nop 0
	s_nop 0
	s_nop 0
	s_nop 0
	s_nop 0
	s_nop 0
	s_nop 0
	s_nop 0

	.amdhsa_kernel _Z8mega_fwd6Params
		.amdhsa_group_segment_fixed_size 0
		.amdhsa_private_segment_fixed_size 0
		.amdhsa_kernarg_size 456
		.amdhsa_user_sgpr_count 2
		.amdhsa_user_sgpr_dispatch_ptr 0
		.amdhsa_user_sgpr_queue_ptr 0
		.amdhsa_user_sgpr_kernarg_segment_ptr 1
		.amdhsa_user_sgpr_dispatch_id 0
		.amdhsa_user_sgpr_kernarg_preload_length 0
		.amdhsa_user_sgpr_kernarg_preload_offset 0
		.amdhsa_user_sgpr_private_segment_size 0
		.amdhsa_uses_dynamic_stack 0
		.amdhsa_enable_private_segment 0
		.amdhsa_system_sgpr_workgroup_id_x 1
		.amdhsa_system_sgpr_workgroup_id_y 0
		.amdhsa_system_sgpr_workgroup_id_z 0
		.amdhsa_system_sgpr_workgroup_info 0
		.amdhsa_system_vgpr_workitem_id 0
		.amdhsa_next_free_vgpr 256
		.amdhsa_next_free_sgpr 102
		.amdhsa_accum_offset 256
		.amdhsa_reserve_vcc 1
		.amdhsa_float_round_mode_32 0
		.amdhsa_float_round_mode_16_64 0
		.amdhsa_float_denorm_mode_32 3
		.amdhsa_float_denorm_mode_16_64 3
		.amdhsa_dx10_clamp 1
		.amdhsa_ieee_mode 1
		.amdhsa_fp16_overflow 0
		.amdhsa_tg_split 0
		.amdhsa_exception_fp_ieee_invalid_op 0
		.amdhsa_exception_fp_denorm_src 0
		.amdhsa_exception_fp_ieee_div_zero 0
		.amdhsa_exception_fp_ieee_overflow 0
		.amdhsa_exception_fp_ieee_underflow 0
		.amdhsa_exception_fp_ieee_inexact 0
		.amdhsa_exception_int_div_zero 0
	.end_amdhsa_kernel

amdhsa.kernels:
  - .agpr_count:     0
    .args:
      - .offset:         0
        .size:           200
        .value_kind:     by_value
      - .offset:         200
        .size:           4
        .value_kind:     hidden_block_count_x
      - .offset:         204
        .size:           4
        .value_kind:     hidden_block_count_y
      - .offset:         208
        .size:           4
        .value_kind:     hidden_block_count_z
      - .offset:         212
        .size:           2
        .value_kind:     hidden_group_size_x
      - .offset:         214
        .size:           2
        .value_kind:     hidden_group_size_y
      - .offset:         216
        .size:           2
        .value_kind:     hidden_group_size_z
      - .offset:         218
        .size:           2
        .value_kind:     hidden_remainder_x
      - .offset:         220
        .size:           2
        .value_kind:     hidden_remainder_y
      - .offset:         222
        .size:           2
        .value_kind:     hidden_remainder_z
      - .offset:         240
        .size:           8
        .value_kind:     hidden_global_offset_x
      - .offset:         248
        .size:           8
        .value_kind:     hidden_global_offset_y
      - .offset:         256
        .size:           8
        .value_kind:     hidden_global_offset_z
      - .offset:         264
        .size:           2
        .value_kind:     hidden_grid_dims
      - .offset:         320
        .size:           4
        .value_kind:     hidden_dynamic_lds_size
    .group_segment_fixed_size: 0
    .kernarg_segment_align: 8
    .kernarg_segment_size: 456
    .language:       OpenCL C
    .language_version:
      - 2
      - 0
    .max_flat_workgroup_size: 512
    .name:           _Z8mega_fwd6Params
    .private_segment_fixed_size: 0
    .sgpr_count:     108
    .sgpr_spill_count: 256
    .symbol:         _Z8mega_fwd6Params.kd
    .uniform_work_group_size: 1
    .uses_dynamic_stack: false
    .vgpr_count:     256
    .vgpr_spill_count: 0
    .wavefront_size: 64
